# baseline (speedup 1.0000x reference)
.LBB2_13:
	v_exp_f32_e32 v48, v48
	v_exp_f32_e32 v49, v49
	v_mfma_f32_32x32x16_bf16 v[112:127], a[192:195], a[128:131], v[16:31]
	ds_read_b64_tr_b16 v[180:181], v223 offset:0
	v_cvt_pk_bf16_f32 v164, v128, v129
	v_exp_f32_e32 v50, v50
	v_exp_f32_e32 v51, v51
	v_mfma_f32_32x32x16_bf16 v[96:111], a[192:195], a[160:163], v[0:15]
	ds_read_b64_tr_b16 v[182:183], v223 offset:0x800
	v_cvt_pk_bf16_f32 v165, v130, v131
	v_mfma_f32_32x32x16_bf16 v[80:95], a[224:227], a[128:131], v[16:31]
	ds_read_b64_tr_b16 v[184:185], v223 offset:0x200
	v_exp_f32_e32 v236, v52
	v_exp_f32_e32 v237, v53
	v_cvt_pk_bf16_f32 v166, v132, v133
	v_mfma_f32_32x32x16_bf16 v[64:79], a[224:227], a[160:163], v[0:15]
	ds_read_b64_tr_b16 v[186:187], v223 offset:0xa00
	ds_read_b64_tr_b16 v[176:177], v223 offset:0x400
	v_exp_f32_e32 v242, v54
	v_exp_f32_e32 v243, v55
	v_cvt_pk_bf16_f32 v167, v134, v135
	v_exp_f32_e32 v198, v56
	v_exp_f32_e32 v199, v57
	v_mfma_f32_32x32x16_bf16 v[112:127], a[196:199], a[132:135], v[112:127]
	ds_read_b64_tr_b16 v[178:179], v223 offset:0xc00
	v_cvt_pk_bf16_f32 v128, v136, v137
	v_exp_f32_e32 v230, v58
	v_exp_f32_e32 v231, v59
	v_mfma_f32_32x32x16_bf16 v[96:111], a[196:199], a[164:167], v[96:111]
	ds_read_b64_tr_b16 v[188:189], v223 offset:0x600
	v_cvt_pk_bf16_f32 v129, v138, v139
	v_exp_f32_e32 v232, v60
	v_exp_f32_e32 v233, v61
	v_mfma_f32_32x32x16_bf16 v[80:95], a[228:231], a[132:135], v[80:95]
	ds_read_b64_tr_b16 v[190:191], v223 offset:0xe00
	v_cvt_pk_bf16_f32 v130, v140, v141
	v_mfma_f32_32x32x16_bf16 v[64:79], a[228:231], a[164:167], v[64:79]
	ds_read_b64_tr_b16 v[172:173], v223 offset:0x1000
	v_exp_f32_e32 v234, v62
	v_exp_f32_e32 v235, v63
	ds_read_b64_tr_b16 v[174:175], v223 offset:0x1800
	v_cvt_pk_bf16_f32 v131, v142, v143
	v_exp_f32_e32 v141, v32
	v_exp_f32_e32 v142, v33
	v_mfma_f32_32x32x16_bf16 v[112:127], a[200:203], a[136:139], v[112:127]
	ds_read_b64_tr_b16 v[168:169], v223 offset:0x1200
	v_cvt_pk_bf16_f32 v192, v144, v145
	v_exp_f32_e32 v143, v34
	v_mfma_f32_32x32x16_bf16 v[96:111], a[200:203], a[168:171], v[96:111]
	ds_read_b64_tr_b16 v[170:171], v223 offset:0x1a00
	v_exp_f32_e32 v244, v35
	v_cvt_pk_bf16_f32 v193, v146, v147
	v_mfma_f32_32x32x16_bf16 v[80:95], a[232:235], a[136:139], v[80:95]
	ds_read_b64_tr_b16 v[160:161], v223 offset:0x1400
	v_exp_f32_e32 v245, v36
	v_exp_f32_e32 v246, v37
	v_cvt_pk_bf16_f32 v194, v148, v149
	v_mfma_f32_32x32x16_bf16 v[64:79], a[232:235], a[168:171], v[64:79]
	ds_read_b64_tr_b16 v[162:163], v223 offset:0x1c00
	ds_read_b64_tr_b16 v[136:137], v223 offset:0x1600
	v_exp_f32_e32 v247, v38
	v_exp_f32_e32 v248, v39
	v_cvt_pk_bf16_f32 v195, v150, v151
	v_exp_f32_e32 v148, v40
	v_exp_f32_e32 v149, v41
	v_mfma_f32_32x32x16_bf16 v[112:127], a[204:207], a[140:143], v[112:127]
	ds_read_b64_tr_b16 v[138:139], v223 offset:0x1e00
	v_cvt_pk_bf16_f32 v144, v152, v153
	v_exp_f32_e32 v150, v42
	v_exp_f32_e32 v151, v43
	v_mfma_f32_32x32x16_bf16 v[96:111], a[204:207], a[172:175], v[96:111]
	ds_read_b64_tr_b16 v[132:133], v223 offset:0x2000
	v_cvt_pk_bf16_f32 v145, v154, v155
	v_exp_f32_e32 v152, v44
	v_exp_f32_e32 v153, v45
	v_mfma_f32_32x32x16_bf16 v[80:95], a[236:239], a[140:143], v[80:95]
	ds_read_b64_tr_b16 v[134:135], v223 offset:0x2800
	v_cvt_pk_bf16_f32 v146, v156, v157
	v_mfma_f32_32x32x16_bf16 v[64:79], a[236:239], a[172:175], v[64:79]
	ds_read_b64_tr_b16 v[60:61], v223 offset:0x2200
	v_exp_f32_e32 v154, v46
	v_exp_f32_e32 v155, v47
	ds_read_b64_tr_b16 v[62:63], v223 offset:0x2a00
	v_cvt_pk_bf16_f32 v147, v158, v159
	v_mfma_f32_32x32x16_bf16 v[112:127], a[208:211], a[144:147], v[112:127]
	ds_read_b64_tr_b16 v[56:57], v223 offset:0x2400
	v_cvt_pk_bf16_f32 v52, v48, v49
	v_add_f32_e32 v32, v239, v48
	v_add_f32_e32 v33, v238, v49
	s_add_i32 s19, s17, 0xfffda000
	v_mfma_f32_32x32x16_bf16 v[96:111], a[208:211], a[176:179], v[96:111]
	ds_read_b64_tr_b16 v[58:59], v223 offset:0x2c00
	v_cvt_pk_bf16_f32 v53, v50, v51
	v_add_f32_e32 v32, v32, v50
	v_add_f32_e32 v33, v33, v51
	v_mfma_f32_32x32x16_bf16 v[80:95], a[240:243], a[144:147], v[80:95]
	ds_read_b64_tr_b16 v[48:49], v223 offset:0x2600
	v_cvt_pk_bf16_f32 v54, v236, v237
	v_add_f32_e32 v32, v32, v236
	v_add_f32_e32 v33, v33, v237
	v_mfma_f32_32x32x16_bf16 v[64:79], a[240:243], a[176:179], v[64:79]
	ds_read_b64_tr_b16 v[50:51], v223 offset:0x2e00
	ds_read_b64_tr_b16 v[44:45], v223 offset:0x3000
	v_cvt_pk_bf16_f32 v55, v242, v243
	v_add_f32_e32 v32, v32, v242
	v_add_f32_e32 v33, v33, v243
	v_mfma_f32_32x32x16_bf16 v[112:127], a[212:215], a[148:151], v[112:127]
	ds_read_b64_tr_b16 v[46:47], v223 offset:0x3800
	v_add_f32_e32 v32, v32, v198
	v_add_f32_e32 v33, v33, v199
	s_add_i32 s24, s17, 0xfffde000
	v_mfma_f32_32x32x16_bf16 v[96:111], a[212:215], a[180:183], v[96:111]
	ds_read_b64_tr_b16 v[40:41], v223 offset:0x3200
	v_add_f32_e32 v32, v32, v230
	v_add_f32_e32 v33, v33, v231
	v_mfma_f32_32x32x16_bf16 v[80:95], a[244:247], a[148:151], v[80:95]
	ds_read_b64_tr_b16 v[42:43], v223 offset:0x3a00
	v_add_f32_e32 v32, v32, v232
	v_add_f32_e32 v33, v33, v233
	v_mfma_f32_32x32x16_bf16 v[64:79], a[244:247], a[180:183], v[64:79]
	ds_read_b64_tr_b16 v[36:37], v223 offset:0x3400
	ds_read_b64_tr_b16 v[38:39], v223 offset:0x3c00
	v_add_f32_e32 v156, v32, v234
	v_add_f32_e32 v157, v33, v235
	v_mfma_f32_32x32x16_bf16 v[112:127], a[216:219], a[152:155], v[112:127]
	ds_read_b64_tr_b16 v[32:33], v223 offset:0x3600
	v_cvt_pk_bf16_f32 v140, v141, v142
	v_add_f32_e32 v158, v240, v141
	v_add_f32_e32 v142, v241, v142
	v_mfma_f32_32x32x16_bf16 v[96:111], a[216:219], a[184:187], v[96:111]
	ds_read_b64_tr_b16 v[34:35], v223 offset:0x3e00
	v_cvt_pk_bf16_f32 v141, v143, v244
	v_add_f32_e32 v143, v158, v143
	v_add_f32_e32 v158, v142, v244
	v_mfma_f32_32x32x16_bf16 v[80:95], a[248:251], a[152:155], v[80:95]
	v_cvt_pk_bf16_f32 v142, v245, v246
	v_add_f32_e32 v159, v143, v245
	v_add_f32_e32 v158, v158, v246
	v_mfma_f32_32x32x16_bf16 v[64:79], a[248:251], a[184:187], v[64:79]
	v_cvt_pk_bf16_f32 v143, v247, v248
	v_add_f32_e32 v159, v159, v247
	v_add_f32_e32 v158, v158, v248
	v_mfma_f32_32x32x16_bf16 v[112:127], a[220:223], a[156:159], v[112:127]
	v_add_f32_e32 v159, v159, v148
	v_add_f32_e32 v158, v158, v149
	v_mfma_f32_32x32x16_bf16 v[96:111], a[220:223], a[188:191], v[96:111]
	v_add_f32_e32 v159, v159, v150
	v_add_f32_e32 v158, v158, v151
	v_mfma_f32_32x32x16_bf16 v[80:95], a[252:255], a[156:159], v[80:95]
	v_add_f32_e32 v159, v159, v152
	v_add_f32_e32 v158, v158, v153
	v_mfma_f32_32x32x16_bf16 v[64:79], a[252:255], a[188:191], v[64:79]
	v_add_f32_e32 v159, v159, v154
	v_add_f32_e32 v158, v158, v155
	s_nop 4
	v_add_f32_e32 v156, v156, v157
	s_waitcnt vmcnt(0) lgkmcnt(0)
	s_barrier
	s_nop 0
	v_mov_b32_e32 v157, v156
	s_nop 1
	v_permlane32_swap_b32_e32 v156, v157
	v_add_f32_e32 v156, v156, v157
	v_add_f32_e32 v197, v197, v156
	v_add_f32_e32 v156, v159, v158
	v_mov_b32_e32 v157, v156
	s_nop 1
	v_permlane32_swap_b32_e32 v156, v157
	v_add_f32_e32 v156, v156, v157
	v_add_f32_e32 v196, v196, v156
	s_nop 1
	v_mfma_f32_32x32x16_bf16 a[0:15], v[180:183], v[164:167], a[0:15]
	s_mov_b32 m0, s30
	s_add_i32 s1, s17, 0xfffda000
	buffer_load_dwordx4 v209, s[4:7], s1 offen lds
	v_mfma_f32_32x32x16_bf16 a[16:31], v[180:183], v[192:195], a[16:31]
	s_mov_b32 m0, s37
	s_add_i32 s82, s17, 0xfffdc000
	buffer_load_dwordx4 v210, s[4:7], s82 offen lds
	ds_read_b128 a[192:195], v219 offset:0
	v_mfma_f32_32x32x16_bf16 a[32:47], v[184:187], v[164:167], a[32:47]
	s_mov_b32 m0, s39
	s_add_i32 s84, s17, 0xfffde000
	buffer_load_dwordx4 v209, s[4:7], s84 offen lds
	ds_read_b128 a[196:199], v220 offset:0
	v_mfma_f32_32x32x16_bf16 a[48:63], v[184:187], v[192:195], a[48:63]
	s_mov_b32 m0, s41
	s_add_i32 s86, s17, 0xfffe0000
	buffer_load_dwordx4 v210, s[4:7], s86 offen lds
	ds_read_b128 a[200:203], v221 offset:0
	v_mfma_f32_32x32x16_bf16 a[64:79], v[176:179], v[164:167], a[64:79]
	s_mov_b32 m0, s43
	s_add_i32 s88, s17, 0xfffba000
	buffer_load_dwordx4 v211, s[20:23], s88 offen lds
	ds_read_b128 a[204:207], v222 offset:0
	v_mfma_f32_32x32x16_bf16 a[80:95], v[176:179], v[192:195], a[80:95]
	s_mov_b32 m0, s45
	s_add_i32 s90, s17, 0xfffba080
	buffer_load_dwordx4 v211, s[20:23], s90 offen lds
	ds_read_b128 a[208:211], v219 offset:128
	v_mfma_f32_32x32x16_bf16 a[96:111], v[188:191], v[164:167], a[96:111]
	s_mov_b32 m0, s47
	s_add_i32 s92, s17, 0xfffbe000
	buffer_load_dwordx4 v211, s[20:23], s92 offen lds
	ds_read_b128 a[212:215], v220 offset:128
	v_mfma_f32_32x32x16_bf16 a[112:127], v[188:191], v[192:195], a[112:127]
	s_mov_b32 m0, s49
	s_add_i32 s94, s17, 0xfffbe080
	buffer_load_dwordx4 v211, s[20:23], s94 offen lds
	ds_read_b128 a[216:219], v221 offset:128
	v_mfma_f32_32x32x16_bf16 a[0:15], v[172:175], v[128:131], a[0:15]
	ds_read_b128 a[220:223], v222 offset:128
	v_max3_f32 v156, v112, v113, v80
	v_max3_f32 v157, v114, v115, v81
	v_max3_f32 v156, v156, v82, v83
	v_mfma_f32_32x32x16_bf16 a[16:31], v[172:175], v[144:147], a[16:31]
	ds_read_b128 a[224:227], v219 offset:8192
	v_max3_f32 v156, v156, v116, v117
	v_max3_f32 v157, v157, v118, v119
	v_max3_f32 v156, v156, v84, v85
	v_max3_f32 v157, v157, v86, v87
	v_mfma_f32_32x32x16_bf16 a[32:47], v[168:171], v[128:131], a[32:47]
	ds_read_b128 a[228:231], v220 offset:8192
	v_max3_f32 v156, v156, v120, v121
	v_max3_f32 v157, v157, v122, v123
	v_max3_f32 v156, v156, v88, v89
	v_max3_f32 v157, v157, v90, v91
	v_mfma_f32_32x32x16_bf16 a[48:63], v[168:171], v[144:147], a[48:63]
	ds_read_b128 a[232:235], v221 offset:8192
	v_max3_f32 v156, v156, v124, v125
	v_max3_f32 v157, v157, v126, v127
	v_max3_f32 v156, v156, v92, v93
	v_max3_f32 v157, v157, v94, v95
	v_mfma_f32_32x32x16_bf16 a[64:79], v[160:163], v[128:131], a[64:79]
	ds_read_b128 a[236:239], v222 offset:8192
	v_max3_f32 v158, v96, v97, v64
	v_max3_f32 v159, v98, v99, v65
	v_max3_f32 v158, v158, v66, v67
	v_mfma_f32_32x32x16_bf16 a[80:95], v[160:163], v[144:147], a[80:95]
	ds_read_b128 a[240:243], v219 offset:8320
	v_max3_f32 v158, v158, v100, v101
	v_max3_f32 v159, v159, v102, v103
	v_max3_f32 v158, v158, v68, v69
	v_max3_f32 v159, v159, v70, v71
	v_mfma_f32_32x32x16_bf16 a[96:111], v[136:139], v[128:131], a[96:111]
	ds_read_b128 a[244:247], v220 offset:8320
	v_max3_f32 v128, v158, v104, v105
	v_max3_f32 v129, v159, v106, v107
	v_max3_f32 v128, v128, v72, v73
	v_max3_f32 v129, v129, v74, v75
	v_mfma_f32_32x32x16_bf16 a[112:127], v[136:139], v[144:147], a[112:127]
	ds_read_b128 a[248:251], v221 offset:8320
	v_max3_f32 v128, v128, v108, v109
	v_max3_f32 v129, v129, v110, v111
	v_max3_f32 v128, v128, v76, v77
	v_max3_f32 v130, v129, v78, v79
	v_mfma_f32_32x32x16_bf16 a[0:15], v[132:135], v[52:55], a[0:15]
	ds_read_b128 a[252:255], v222 offset:8320
	v_max_f32_e32 v129, v156, v157
	v_mov_b32_e32 v131, v129
	s_nop 1
	v_permlane32_swap_b32_e32 v129, v131
	v_max_f32_e32 v129, v129, v131
	v_mfma_f32_32x32x16_bf16 a[16:31], v[132:135], v[140:143], a[16:31]
	v_max_f32_e32 v128, v128, v130
	v_mov_b32_e32 v130, v128
	s_nop 1
	v_permlane32_swap_b32_e32 v128, v130
	v_max_f32_e32 v128, v128, v130
	v_max_f32_e32 v130, v129, v129
	v_max_f32_e32 v131, v128, v128
	v_max_f32_e32 v130, v130, v131
	v_mfma_f32_32x32x16_bf16 a[32:47], v[60:63], v[52:55], a[32:47]
	v_cmp_lt_f32_e32 vcc, s79, v130
	s_cmp_lg_u64 vcc, 0
	s_cselect_b64 s[0:1], -1, 0
	s_cbranch_vccnz .LBB2_18

.LBB2_15:
	s_waitcnt lgkmcnt(0)
	v_exp_f32_e32 v80, v80
	v_exp_f32_e32 v81, v81
	v_mfma_f32_32x32x16_bf16 v[112:127], a[192:195], a[128:131], v[16:31]
	ds_read_b64_tr_b16 v[180:181], v208 offset:0
	v_cvt_pk_bf16_f32 v164, v128, v129
	v_exp_f32_e32 v82, v82
	v_exp_f32_e32 v83, v83
	v_mfma_f32_32x32x16_bf16 v[96:111], a[192:195], a[160:163], v[0:15]
	ds_read_b64_tr_b16 v[182:183], v208 offset:0x800
	v_cvt_pk_bf16_f32 v165, v130, v131
	v_mfma_f32_32x32x16_bf16 v[48:63], a[224:227], a[128:131], v[16:31]
	ds_read_b64_tr_b16 v[184:185], v208 offset:0x200
	v_exp_f32_e32 v240, v84
	v_exp_f32_e32 v241, v85
	v_cvt_pk_bf16_f32 v166, v132, v133
	v_mfma_f32_32x32x16_bf16 v[32:47], a[224:227], a[160:163], v[0:15]
	ds_read_b64_tr_b16 v[186:187], v208 offset:0xa00
	ds_read_b64_tr_b16 v[176:177], v208 offset:0x400
	v_exp_f32_e32 v242, v86
	v_exp_f32_e32 v243, v87
	v_cvt_pk_bf16_f32 v167, v134, v135
	v_exp_f32_e32 v198, v88
	v_exp_f32_e32 v199, v89
	v_mfma_f32_32x32x16_bf16 v[112:127], a[196:199], a[132:135], v[112:127]
	ds_read_b64_tr_b16 v[178:179], v208 offset:0xc00
	v_cvt_pk_bf16_f32 v128, v136, v137
	v_exp_f32_e32 v230, v90
	v_exp_f32_e32 v231, v91
	v_mfma_f32_32x32x16_bf16 v[96:111], a[196:199], a[164:167], v[96:111]
	ds_read_b64_tr_b16 v[188:189], v208 offset:0x600
	v_cvt_pk_bf16_f32 v129, v138, v139
	v_exp_f32_e32 v232, v92
	v_exp_f32_e32 v233, v93
	v_mfma_f32_32x32x16_bf16 v[48:63], a[228:231], a[132:135], v[48:63]
	ds_read_b64_tr_b16 v[190:191], v208 offset:0xe00
	v_cvt_pk_bf16_f32 v130, v140, v141
	v_mfma_f32_32x32x16_bf16 v[32:47], a[228:231], a[164:167], v[32:47]
	ds_read_b64_tr_b16 v[172:173], v208 offset:0x1000
	v_exp_f32_e32 v234, v94
	v_exp_f32_e32 v235, v95
	ds_read_b64_tr_b16 v[174:175], v208 offset:0x1800
	v_cvt_pk_bf16_f32 v131, v142, v143
	v_exp_f32_e32 v141, v64
	v_exp_f32_e32 v142, v65
	v_mfma_f32_32x32x16_bf16 v[112:127], a[200:203], a[136:139], v[112:127]
	ds_read_b64_tr_b16 v[168:169], v208 offset:0x1200
	v_cvt_pk_bf16_f32 v192, v144, v145
	v_exp_f32_e32 v143, v66
	v_mfma_f32_32x32x16_bf16 v[96:111], a[200:203], a[168:171], v[96:111]
	ds_read_b64_tr_b16 v[170:171], v208 offset:0x1a00
	v_exp_f32_e32 v244, v67
	v_cvt_pk_bf16_f32 v193, v146, v147
	v_mfma_f32_32x32x16_bf16 v[48:63], a[232:235], a[136:139], v[48:63]
	ds_read_b64_tr_b16 v[160:161], v208 offset:0x1400
	v_exp_f32_e32 v245, v68
	v_exp_f32_e32 v246, v69
	v_cvt_pk_bf16_f32 v194, v148, v149
	v_mfma_f32_32x32x16_bf16 v[32:47], a[232:235], a[168:171], v[32:47]
	ds_read_b64_tr_b16 v[162:163], v208 offset:0x1c00
	ds_read_b64_tr_b16 v[136:137], v208 offset:0x1600
	v_exp_f32_e32 v247, v70
	v_exp_f32_e32 v248, v71
	v_cvt_pk_bf16_f32 v195, v150, v151
	v_exp_f32_e32 v148, v72
	v_exp_f32_e32 v149, v73
	v_mfma_f32_32x32x16_bf16 v[112:127], a[204:207], a[140:143], v[112:127]
	ds_read_b64_tr_b16 v[138:139], v208 offset:0x1e00
	v_cvt_pk_bf16_f32 v144, v152, v153
	v_exp_f32_e32 v150, v74
	v_exp_f32_e32 v151, v75
	v_mfma_f32_32x32x16_bf16 v[96:111], a[204:207], a[172:175], v[96:111]
	ds_read_b64_tr_b16 v[132:133], v208 offset:0x2000
	v_cvt_pk_bf16_f32 v145, v154, v155
	v_exp_f32_e32 v152, v76
	v_exp_f32_e32 v153, v77
	v_mfma_f32_32x32x16_bf16 v[48:63], a[236:239], a[140:143], v[48:63]
	ds_read_b64_tr_b16 v[134:135], v208 offset:0x2800
	v_cvt_pk_bf16_f32 v146, v156, v157
	v_mfma_f32_32x32x16_bf16 v[32:47], a[236:239], a[172:175], v[32:47]
	ds_read_b64_tr_b16 v[92:93], v208 offset:0x2200
	v_exp_f32_e32 v154, v78
	v_exp_f32_e32 v155, v79
	ds_read_b64_tr_b16 v[94:95], v208 offset:0x2a00
	v_cvt_pk_bf16_f32 v147, v158, v159
	v_mfma_f32_32x32x16_bf16 v[112:127], a[208:211], a[144:147], v[112:127]
	ds_read_b64_tr_b16 v[88:89], v208 offset:0x2400
	v_cvt_pk_bf16_f32 v84, v80, v81
	v_add_f32_e32 v64, v237, v80
	v_add_f32_e32 v65, v236, v81
	v_mfma_f32_32x32x16_bf16 v[96:111], a[208:211], a[176:179], v[96:111]
	ds_read_b64_tr_b16 v[90:91], v208 offset:0x2c00
	v_cvt_pk_bf16_f32 v85, v82, v83
	v_add_f32_e32 v64, v64, v82
	v_add_f32_e32 v65, v65, v83
	v_mfma_f32_32x32x16_bf16 v[48:63], a[240:243], a[144:147], v[48:63]
	ds_read_b64_tr_b16 v[80:81], v208 offset:0x2600
	v_cvt_pk_bf16_f32 v86, v240, v241
	v_add_f32_e32 v64, v64, v240
	v_add_f32_e32 v65, v65, v241
	v_mfma_f32_32x32x16_bf16 v[32:47], a[240:243], a[176:179], v[32:47]
	ds_read_b64_tr_b16 v[82:83], v208 offset:0x2e00
	ds_read_b64_tr_b16 v[76:77], v208 offset:0x3000
	v_cvt_pk_bf16_f32 v87, v242, v243
	v_add_f32_e32 v64, v64, v242
	v_add_f32_e32 v65, v65, v243
	v_mfma_f32_32x32x16_bf16 v[112:127], a[212:215], a[148:151], v[112:127]
	ds_read_b64_tr_b16 v[78:79], v208 offset:0x3800
	v_add_f32_e32 v64, v64, v198
	v_add_f32_e32 v65, v65, v199
	v_mfma_f32_32x32x16_bf16 v[96:111], a[212:215], a[180:183], v[96:111]
	ds_read_b64_tr_b16 v[72:73], v208 offset:0x3200
	v_add_f32_e32 v64, v64, v230
	v_add_f32_e32 v65, v65, v231
	v_mfma_f32_32x32x16_bf16 v[48:63], a[244:247], a[148:151], v[48:63]
	ds_read_b64_tr_b16 v[74:75], v208 offset:0x3a00
	v_add_f32_e32 v64, v64, v232
	v_add_f32_e32 v65, v65, v233
	v_mfma_f32_32x32x16_bf16 v[32:47], a[244:247], a[180:183], v[32:47]
	ds_read_b64_tr_b16 v[68:69], v208 offset:0x3400
	ds_read_b64_tr_b16 v[70:71], v208 offset:0x3c00
	v_add_f32_e32 v156, v64, v234
	v_add_f32_e32 v157, v65, v235
	v_mfma_f32_32x32x16_bf16 v[112:127], a[216:219], a[152:155], v[112:127]
	ds_read_b64_tr_b16 v[64:65], v208 offset:0x3600
	v_cvt_pk_bf16_f32 v140, v141, v142
	v_add_f32_e32 v158, v238, v141
	v_add_f32_e32 v142, v239, v142
	v_mfma_f32_32x32x16_bf16 v[96:111], a[216:219], a[184:187], v[96:111]
	ds_read_b64_tr_b16 v[66:67], v208 offset:0x3e00
	v_cvt_pk_bf16_f32 v141, v143, v244
	v_add_f32_e32 v143, v158, v143
	v_add_f32_e32 v158, v142, v244
	v_mfma_f32_32x32x16_bf16 v[48:63], a[248:251], a[152:155], v[48:63]
	v_cvt_pk_bf16_f32 v142, v245, v246
	v_add_f32_e32 v159, v143, v245
	v_add_f32_e32 v158, v158, v246
	v_mfma_f32_32x32x16_bf16 v[32:47], a[248:251], a[184:187], v[32:47]
	v_cvt_pk_bf16_f32 v143, v247, v248
	v_add_f32_e32 v159, v159, v247
	v_add_f32_e32 v158, v158, v248
	v_mfma_f32_32x32x16_bf16 v[112:127], a[220:223], a[156:159], v[112:127]
	v_add_f32_e32 v159, v159, v148
	v_add_f32_e32 v158, v158, v149
	v_mfma_f32_32x32x16_bf16 v[96:111], a[220:223], a[188:191], v[96:111]
	v_add_f32_e32 v159, v159, v150
	v_add_f32_e32 v158, v158, v151
	v_mfma_f32_32x32x16_bf16 v[48:63], a[252:255], a[156:159], v[48:63]
	v_add_f32_e32 v159, v159, v152
	v_add_f32_e32 v158, v158, v153
	v_mfma_f32_32x32x16_bf16 v[32:47], a[252:255], a[188:191], v[32:47]
	v_add_f32_e32 v159, v159, v154
	v_add_f32_e32 v158, v158, v155
	s_nop 4
	v_add_f32_e32 v156, v156, v157
	s_waitcnt vmcnt(0) lgkmcnt(0)
	s_barrier
	s_nop 0
	v_mov_b32_e32 v157, v156
	s_nop 1
	v_permlane32_swap_b32_e32 v156, v157
	v_add_f32_e32 v156, v156, v157
	v_add_f32_e32 v197, v197, v156
	v_add_f32_e32 v156, v159, v158
	v_mov_b32_e32 v157, v156
	s_nop 1
	v_permlane32_swap_b32_e32 v156, v157
	v_add_f32_e32 v156, v156, v157
	v_add_f32_e32 v196, v196, v156
	s_nop 1
	v_mfma_f32_32x32x16_bf16 a[0:15], v[180:183], v[164:167], a[0:15]
	s_mov_b32 m0, s51
	s_add_i32 s1, s17, 0xffffa000
	buffer_load_dwordx4 v209, s[4:7], s1 offen lds
	v_mfma_f32_32x32x16_bf16 a[16:31], v[180:183], v[192:195], a[16:31]
	s_mov_b32 m0, s53
	s_add_i32 s82, s17, 0xffffc000
	buffer_load_dwordx4 v210, s[4:7], s82 offen lds
	ds_read_b128 a[192:195], v204 offset:0
	v_mfma_f32_32x32x16_bf16 a[32:47], v[184:187], v[164:167], a[32:47]
	s_mov_b32 m0, s55
	s_add_i32 s84, s17, 0xffffe000
	buffer_load_dwordx4 v209, s[4:7], s84 offen lds
	ds_read_b128 a[196:199], v205 offset:0
	v_mfma_f32_32x32x16_bf16 a[48:63], v[184:187], v[192:195], a[48:63]
	s_mov_b32 m0, s57
	s_nop 0
	buffer_load_dwordx4 v210, s[4:7], s17 offen lds
	ds_read_b128 a[200:203], v206 offset:0
	v_mfma_f32_32x32x16_bf16 a[64:79], v[176:179], v[164:167], a[64:79]
	s_mov_b32 m0, s31
	s_nop 0
	buffer_load_dwordx4 v211, s[20:23], s19 offen lds
	ds_read_b128 a[204:207], v207 offset:0
	v_mfma_f32_32x32x16_bf16 a[80:95], v[176:179], v[192:195], a[80:95]
	s_mov_b32 m0, s59
	s_add_i32 s89, s17, 0xfffda080
	buffer_load_dwordx4 v211, s[20:23], s89 offen lds
	ds_read_b128 a[208:211], v204 offset:128
	v_mfma_f32_32x32x16_bf16 a[96:111], v[188:191], v[164:167], a[96:111]
	s_mov_b32 m0, s61
	s_nop 0
	buffer_load_dwordx4 v211, s[20:23], s24 offen lds
	ds_read_b128 a[212:215], v205 offset:128
	v_mfma_f32_32x32x16_bf16 a[112:127], v[188:191], v[192:195], a[112:127]
	s_mov_b32 m0, s62
	s_add_i32 s92, s17, 0xfffde080
	buffer_load_dwordx4 v211, s[20:23], s92 offen lds
	ds_read_b128 a[216:219], v206 offset:128
	v_mfma_f32_32x32x16_bf16 a[0:15], v[172:175], v[128:131], a[0:15]
	ds_read_b128 a[220:223], v207 offset:128
	v_max3_f32 v156, v112, v113, v48
	v_max3_f32 v157, v114, v115, v49
	v_max3_f32 v156, v156, v50, v51
	v_mfma_f32_32x32x16_bf16 a[16:31], v[172:175], v[144:147], a[16:31]
	ds_read_b128 a[224:227], v204 offset:8192
	v_max3_f32 v156, v156, v116, v117
	v_max3_f32 v157, v157, v118, v119
	v_max3_f32 v156, v156, v52, v53
	v_max3_f32 v157, v157, v54, v55
	v_mfma_f32_32x32x16_bf16 a[32:47], v[168:171], v[128:131], a[32:47]
	ds_read_b128 a[228:231], v205 offset:8192
	v_max3_f32 v156, v156, v120, v121
	v_max3_f32 v157, v157, v122, v123
	v_max3_f32 v156, v156, v56, v57
	v_max3_f32 v157, v157, v58, v59
	v_mfma_f32_32x32x16_bf16 a[48:63], v[168:171], v[144:147], a[48:63]
	ds_read_b128 a[232:235], v206 offset:8192
	v_max3_f32 v156, v156, v124, v125
	v_max3_f32 v157, v157, v126, v127
	v_max3_f32 v156, v156, v60, v61
	v_max3_f32 v157, v157, v62, v63
	v_mfma_f32_32x32x16_bf16 a[64:79], v[160:163], v[128:131], a[64:79]
	ds_read_b128 a[236:239], v207 offset:8192
	v_max3_f32 v158, v96, v97, v32
	v_max3_f32 v159, v98, v99, v33
	v_max3_f32 v158, v158, v34, v35
	v_mfma_f32_32x32x16_bf16 a[80:95], v[160:163], v[144:147], a[80:95]
	ds_read_b128 a[240:243], v204 offset:8320
	v_max3_f32 v158, v158, v100, v101
	v_max3_f32 v159, v159, v102, v103
	v_max3_f32 v158, v158, v36, v37
	v_max3_f32 v159, v159, v38, v39
	v_mfma_f32_32x32x16_bf16 a[96:111], v[136:139], v[128:131], a[96:111]
	ds_read_b128 a[244:247], v205 offset:8320
	v_max3_f32 v128, v158, v104, v105
	v_max3_f32 v129, v159, v106, v107
	v_max3_f32 v128, v128, v40, v41
	v_max3_f32 v129, v129, v42, v43
	v_mfma_f32_32x32x16_bf16 a[112:127], v[136:139], v[144:147], a[112:127]
	ds_read_b128 a[248:251], v206 offset:8320
	v_max3_f32 v128, v128, v108, v109
	v_max3_f32 v129, v129, v110, v111
	v_max3_f32 v128, v128, v44, v45
	v_max3_f32 v130, v129, v46, v47
	v_mfma_f32_32x32x16_bf16 a[0:15], v[132:135], v[84:87], a[0:15]
	ds_read_b128 a[252:255], v207 offset:8320
	v_max_f32_e32 v129, v156, v157
	v_mov_b32_e32 v131, v129
	s_nop 1
	v_permlane32_swap_b32_e32 v129, v131
	v_max_f32_e32 v129, v129, v131
	v_mfma_f32_32x32x16_bf16 a[16:31], v[132:135], v[140:143], a[16:31]
	v_max_f32_e32 v128, v128, v130
	v_mov_b32_e32 v130, v128
	s_nop 1
	v_permlane32_swap_b32_e32 v128, v130
	v_max_f32_e32 v128, v128, v130
	v_max_f32_e32 v130, v129, v129
	v_max_f32_e32 v131, v128, v128
	v_max_f32_e32 v130, v130, v131
	v_mfma_f32_32x32x16_bf16 a[32:47], v[92:95], v[84:87], a[32:47]
	v_cmp_lt_f32_e32 vcc, s79, v130
	s_cmp_lg_u64 vcc, 0
	s_cselect_b64 s[0:1], -1, 0
	s_cbranch_vccnz .LBB2_20
